# k35: k33 + P3->P5 grid barrier split into arrive (end of P3) and wait (in front of P5's pool-out GEMM, the first consumer of other workgroups' P3 output); the carry scan and SSM output GEMM run in bet
# speedup vs baseline: 1.0077x; 1.0024x over previous
; __device__ __forceinline__ unsigned xb_ld(unsigned* p)              { return __hip_atomic_load(p, __ATOMIC_RELAXED, __HIP_MEMORY_SCOPE_AGENT); }
; __device__ __forceinline__ unsigned xb_add(unsigned* p, unsigned v) { return __hip_atomic_fetch_add(p, v, __ATOMIC_RELAXED, __HIP_MEMORY_SCOPE_AGENT); }
; #define XB_SPIN(cond, bar) do { unsigned _sp = 0; while (cond) { __builtin_amdgcn_s_sleep(1); \
;     if ((++_sp & 255u) == 0u) { if (xb_ld(&(bar)[XB_TMO])) break; if (_sp > XB_SPIN_CAP) { atomicAdd(&(bar)[XB_TMO], 1u); break; } } } } while (0)
; #define GRID_BAR() do { if (N_LAUNCHES == 1) xcd_barrier(bar); } while (0)
; #define BOTH(k) (IN(k) && IN((k) + 1))
; #define PROBE_MID(k) do { if (PROBE_PH == (k) && PROBE_MODE == 0) { __syncthreads(); pr_dt = __builtin_amdgcn_s_memrealtime() - pr_t0; } } while (0)
; #define PROBE_END(k) do { if (PROBE_PH == (k) && PROBE_MODE == 1) { pr_dt = __builtin_amdgcn_s_memrealtime() - pr_t0; } } while (0)
; __device__ __forceinline__ void xcd_barrier(const XcdBarrier& b) {
;     asm volatile("s_waitcnt vmcnt(0)" ::: "memory");
;     __syncthreads();
;     if (threadIdx.x == 0) {
;         unsigned* bar = b.bar;
;         __builtin_amdgcn_s_waitcnt(0);
;         unsigned nloc = b.st[0], nx = b.st[1];
;         if (nloc == 0u) { xcd_barrier_complete(bar, b.x, nloc, nx); b.st[0] = nloc; b.st[1] = nx; }
;         const unsigned old = xb_add(&bar[XB_XSUB(b.x)], 1u);
;         const unsigned gen = old / nloc;
;         if (old + 1u == (gen + 1u) * nloc) {
;             __builtin_amdgcn_fence(__ATOMIC_RELEASE, "agent");
;             asm volatile("s_waitcnt vmcnt(0)" ::: "memory");
;             const unsigned og = xb_add(&bar[XB_TOP], 1u);
;             const unsigned tg = og / nx;
;             if (og + 1u == (tg + 1u) * nx) xb_add(&bar[XB_TOPGEN], 1u);
;             else XB_SPIN(xb_ld(&bar[XB_TOPGEN]) == tg, bar);
; __global__ void __launch_bounds__(NWAVES * 64, 2) fwd_kernel(Args args) {
;     ...
;         PROBE_MID(3); if (BOTH(3)) GRID_BAR(); PROBE_END(3);
.LBB0_691:
	s_cmp_gt_i32 s95, 4
	s_cbranch_scc0 .LBB0_745
	v_readlane_b32 s98, v254, 40
	s_cmp_lg_u32 s98, 0
	s_cbranch_scc1 .Lb4_full
	s_cmpk_lg_i32 s50, 0x100
	s_cbranch_scc1 .Lb4_full
	s_waitcnt vmcnt(0)
	s_barrier
	s_and_saveexec_b64 s[4:5], s[88:89]
	s_cbranch_execz .Lb4_arr_done
	s_lshl_b32 s3, s0, 8
	s_add_u32 s6, s96, s3
	s_addc_u32 s7, s97, 0
	v_mov_b32_e32 v1, 0x1000
	v_mov_b32_e32 v2, 1
	global_atomic_add v1, v1, v2, s[6:7] offset:1024 sc0
	s_waitcnt vmcnt(0)
	v_readfirstlane_b32 s3, v1
	s_add_i32 s3, s3, 1
	s_and_b32 s3, s3, 31
	s_cmp_eq_u32 s3, 0
	s_cbranch_scc0 .Lb4_arr_done
	buffer_wbl2 sc1
	s_waitcnt vmcnt(0)
	v_mov_b32_e32 v1, 0x2000
	global_atomic_add v1, v2, s[6:7] offset:1024
	v_mov_b32_e32 v1, 0x3400
	global_atomic_add v1, v1, v2, s[96:97] sc0
	s_waitcnt vmcnt(0)
	v_readfirstlane_b32 s3, v1
	s_add_i32 s3, s3, 1
	s_and_b32 s3, s3, 7
	s_cmp_eq_u32 s3, 0
	s_cbranch_scc0 .Lb4_arr_done
	v_mov_b32_e32 v1, 0x3500
	global_atomic_add v1, v2, s[96:97]
.Lb4_arr_done:
	s_or_b64 exec, exec, s[4:5]
	s_branch .LBB0_745
.Lb4_full:
	s_waitcnt vmcnt(0)
	s_waitcnt vmcnt(0)
	s_barrier
	s_and_saveexec_b64 s[4:5], s[88:89]
	s_cbranch_execz .LBB0_744
	s_add_i32 s3, 0, 0x20160
	v_mov_b32_e32 v1, s3
	s_waitcnt vmcnt(0) expcnt(0) lgkmcnt(0)
	ds_read_b32 v3, v1
	s_add_i32 s3, 0, 0x20164
	v_mov_b32_e32 v1, s3
	ds_read_b32 v1, v1
	s_waitcnt lgkmcnt(1)
	v_cmp_ne_u32_e32 vcc, 0, v3
	s_cbranch_vccnz .LBB0_708
	v_readlane_b32 s6, v254, 3
	v_readlane_b32 s7, v254, 4
	s_load_dwordx2 s[10:11], s[6:7], 0x4
	v_readlane_b32 s34, v254, 5
	v_readlane_b32 s35, v254, 6
	s_add_u32 s6, s34, 0x4200
	s_addc_u32 s7, s35, 0
	s_add_u32 s8, s34, 0x4400
	s_addc_u32 s9, s35, 0
	s_waitcnt lgkmcnt(0)
	s_mul_i32 s3, s10, s50
	s_add_u32 s10, s34, 0x4500
	s_mul_i32 s3, s3, s11
	s_addc_u32 s11, s35, 0
	s_add_u32 s12, s34, 0x4600
	s_addc_u32 s13, s35, 0
	s_add_u32 s14, s34, 0x4700
	s_addc_u32 s15, s35, 0
	s_add_u32 s16, s34, 0x4800
	s_addc_u32 s17, s35, 0
	s_add_u32 s18, s34, 0x4900
	s_addc_u32 s19, s35, 0
	s_add_u32 s20, s34, 0x4a00
	s_addc_u32 s21, s35, 0
	s_add_u32 s22, s34, 0x4b00
	s_addc_u32 s23, s35, 0
	s_add_u32 s24, s34, 0x4c00
	s_addc_u32 s25, s35, 0
	s_add_u32 s26, s34, 0x4d00
	s_addc_u32 s27, s35, 0
	s_add_u32 s28, s34, 0x4e00
	s_addc_u32 s29, s35, 0
	s_add_u32 s30, s34, 0x4f00
	s_addc_u32 s31, s35, 0
	s_add_u32 s36, s34, 0x5000
	s_addc_u32 s37, s35, 0
	s_add_u32 s38, s34, 0x5100
	s_addc_u32 s39, s35, 0
	s_add_u32 s40, s34, 0x5200
	s_addc_u32 s41, s35, 0
	s_add_u32 s42, s34, 0x5300
	s_addc_u32 s43, s35, 0
	s_mov_b32 s33, 1
	v_mov_b32_e32 v17, 0
	s_branch .LBB0_696

; __device__ __forceinline__ unsigned xb_ld(unsigned* p)              { return __hip_atomic_load(p, __ATOMIC_RELAXED, __HIP_MEMORY_SCOPE_AGENT); }
; __device__ __forceinline__ unsigned xb_add(unsigned* p, unsigned v) { return __hip_atomic_fetch_add(p, v, __ATOMIC_RELAXED, __HIP_MEMORY_SCOPE_AGENT); }
; #define XB_SPIN(cond, bar) do { unsigned _sp = 0; while (cond) { __builtin_amdgcn_s_sleep(1); \
;     if ((++_sp & 255u) == 0u) { if (xb_ld(&(bar)[XB_TMO])) break; if (_sp > XB_SPIN_CAP) { atomicAdd(&(bar)[XB_TMO], 1u); break; } } } } while (0)
; __device__ __forceinline__ void xcd_barrier(const XcdBarrier& b) {
;     ...
;             else XB_SPIN(xb_ld(&bar[XB_TOPGEN]) == tg, bar);
;             __builtin_amdgcn_fence(__ATOMIC_ACQUIRE, "agent");
;             xb_add(&bar[XB_XGEN(b.x)], 1u);
;             asm volatile("s_waitcnt vmcnt(0)" ::: "memory");
;         } else {
;             XB_SPIN(xb_ld(&bar[XB_XGEN(b.x)]) == gen, bar);
;             __builtin_amdgcn_fence(__ATOMIC_ACQUIRE, "agent");
;             asm volatile("s_waitcnt vmcnt(0)" ::: "memory");
; __global__ void __launch_bounds__(NWAVES * 64, 2) fwd_kernel(Args args) {
;     ...
;         { SchedDense S; S.init(PM, WpoT, T, D, PW, PW, G, bx, PO_FP8 ? 1 : 2);
.LBB0_787:
	v_readlane_b32 s98, v254, 40
	s_cmp_lg_u32 s98, 0
	s_cbranch_scc1 .Lb4_nowait
	s_cmpk_lg_i32 s50, 0x100
	s_cbranch_scc1 .Lb4_nowait
	s_cmp_gt_i32 s95, 4
	s_cbranch_scc0 .Lb4_nowait
	s_and_saveexec_b64 s[100:101], s[88:89]
	s_cbranch_execz .Lb4_wait_done
	s_mov_b32 s98, 0
	v_mov_b32_e32 v252, 0x3500
.Lb4_poll:
	global_load_dword v253, v252, s[96:97] sc1
	s_waitcnt vmcnt(0)
	v_readfirstlane_b32 s99, v253
	s_cmp_ge_u32 s99, 4
	s_cbranch_scc1 .Lb4_seen
	s_sleep 1
	s_add_i32 s98, s98, 1
	s_cmp_lt_u32 s98, 0x100000
	s_cbranch_scc1 .Lb4_poll
.Lb4_seen:
	buffer_inv sc1
	s_waitcnt vmcnt(0)
.Lb4_wait_done:
	s_or_b64 exec, exec, s[100:101]
	s_barrier
